# speedup vs baseline: 1.0102x; 1.0015x over previous
.Lmk_start:
	s_mov_b32 s28, s8
	s_mov_b64 s[30:31], s[4:5]
	s_mov_b64 s[32:33], s[6:7]
	s_mov_b64 s[6:7], s[2:3]
	s_mov_b64 s[34:35], s[2:3]
	s_mov_b32 s2, s28
	s_and_b32 s3, s2, 7
	s_lshr_b32 s4, s2, 3
	s_and_b32 s5, s4, 3
	s_lshl_b32 s3, s3, 2
	s_or_b32 s8, s3, s5
	s_lshr_b32 s9, s4, 2
	v_lshrrev_b32_e32 v127, 6, v0
	v_and_b32_e32 v124, 63, v0
	v_lshlrev_b32_e32 v125, 3, v124
	v_lshlrev_b32_e32 v124, 4, v124
	v_readfirstlane_b32 s12, v127
	v_mov_b32_e32 v120, 0
	v_mov_b32_e32 v121, 0
	v_mov_b32_e32 v122, 0
	v_mov_b32_e32 v123, 0
	s_lshl_b32 s13, s12, 10
	s_lshl_b32 s14, s9, 3
	s_add_u32 s14, s14, s12
	s_mul_i32 s15, s14, 0x1800
	s_mul_i32 s16, s8, 0x12000
	s_add_u32 s16, s16, 0xc0000
	s_add_u32 s16, s16, s13
	s_add_u32 s20, s13, 0x2000
	s_add_u32 s10, s6, s16
	s_addc_u32 s11, s7, 0
	s_add_u32 s18, s6, s15
	s_addc_u32 s19, s7, 0
	s_add_u32 s22, s18, 0x1000
	s_addc_u32 s23, s19, 0
	s_cmp_lt_u32 s12, 4
	s_cbranch_scc0 .Lmk_vb
	s_mov_b32 m0, s13
	s_nop 0
	global_load_lds_dwordx4 v124, s[10:11]
	s_add_u32 s26, s10, 0x2000
	s_addc_u32 s27, s11, 0
	s_mov_b32 m0, s20
	s_nop 0
	global_load_lds_dwordx4 v124, s[26:27]
	global_load_dwordx4 v[96:99], v124, s[18:19]
	global_load_dwordx2 v[100:101], v125, s[22:23]
	global_load_dwordx4 v[102:105], v124, s[18:19] offset:1024
	global_load_dwordx2 v[106:107], v125, s[22:23] offset:512
	global_load_dwordx4 v[108:111], v124, s[18:19] offset:2048
	global_load_dwordx2 v[112:113], v125, s[22:23] offset:1024
	global_load_dwordx4 v[114:117], v124, s[18:19] offset:3072
	global_load_dwordx2 v[118:119], v125, s[22:23] offset:1536
	s_add_u32 s24, s10, 0x3000
	s_addc_u32 s25, s11, 0
	s_add_u32 s26, s13, 0x3000
	s_mov_b32 m0, s26
	s_nop 0
	global_load_lds_dwordx4 v124, s[24:25]
	s_add_u32 s26, s24, 0x2000
	s_addc_u32 s27, s25, 0
	s_add_u32 s29, s20, 0x3000
	s_mov_b32 m0, s29
	s_nop 0
	global_load_lds_dwordx4 v124, s[26:27]
	s_add_u32 s24, s10, 0x6000
	s_addc_u32 s25, s11, 0
	s_add_u32 s26, s13, 0x6000
	s_mov_b32 m0, s26
	s_nop 0
	global_load_lds_dwordx4 v124, s[24:25]
	s_add_u32 s26, s24, 0x2000
	s_addc_u32 s27, s25, 0
	s_add_u32 s29, s20, 0x6000
	s_mov_b32 m0, s29
	s_nop 0
	global_load_lds_dwordx4 v124, s[26:27]
	s_add_u32 s24, s10, 0x9000
	s_addc_u32 s25, s11, 0
	s_add_u32 s26, s13, 0x9000
	s_mov_b32 m0, s26
	s_nop 0
	global_load_lds_dwordx4 v124, s[24:25]
	s_add_u32 s26, s24, 0x2000
	s_addc_u32 s27, s25, 0
	s_add_u32 s29, s20, 0x9000
	s_mov_b32 m0, s29
	s_nop 0
	global_load_lds_dwordx4 v124, s[26:27]
	s_add_u32 s24, s10, 0xc000
	s_addc_u32 s25, s11, 0
	s_add_u32 s26, s13, 0xc000
	s_mov_b32 m0, s26
	s_nop 0
	global_load_lds_dwordx4 v124, s[24:25]
	s_add_u32 s26, s24, 0x2000
	s_addc_u32 s27, s25, 0
	s_add_u32 s29, s20, 0xc000
	s_mov_b32 m0, s29
	s_nop 0
	global_load_lds_dwordx4 v124, s[26:27]
	s_waitcnt vmcnt(8)
	s_barrier
	ds_read_b128 v[0:3], v124
	ds_read_b64 v[4:5], v125 offset:4096
	ds_read_b128 v[6:9], v124 offset:1024
	ds_read_b64 v[10:11], v125 offset:4608
	ds_read_b128 v[12:15], v124 offset:2048
	ds_read_b64 v[16:17], v125 offset:5120
	ds_read_b128 v[18:21], v124 offset:3072
	ds_read_b64 v[22:23], v125 offset:5632
	s_waitcnt lgkmcnt(0)
	s_setprio 2
	v_mfma_f32_32x32x64_f8f6f4 v[48:63], v[0:5], v[96:101], 0 cbsz:2 blgp:2
	ds_read_b128 v[24:27], v124 offset:6144
	ds_read_b64 v[28:29], v125 offset:10240
	v_mfma_f32_32x32x64_f8f6f4 v[48:63], v[6:11], v[102:107], v[48:63] cbsz:2 blgp:2
	ds_read_b128 v[30:33], v124 offset:7168
	ds_read_b64 v[34:35], v125 offset:10752
	v_mfma_f32_32x32x64_f8f6f4 v[48:63], v[12:17], v[108:113], v[48:63] cbsz:2 blgp:2
	ds_read_b128 v[36:39], v124 offset:8192
	ds_read_b64 v[40:41], v125 offset:11264
	v_mfma_f32_32x32x64_f8f6f4 v[48:63], v[18:23], v[114:119], v[48:63] cbsz:2 blgp:2
	ds_read_b128 v[42:45], v124 offset:9216
	ds_read_b64 v[46:47], v125 offset:11776
	s_waitcnt vmcnt(6) lgkmcnt(0)
	s_barrier
	s_add_u32 s24, s10, 0xf000
	s_addc_u32 s25, s11, 0
	s_mov_b32 m0, s13
	s_nop 0
	global_load_lds_dwordx4 v124, s[24:25]
	s_add_u32 s26, s24, 0x2000
	s_addc_u32 s27, s25, 0
	s_mov_b32 m0, s20
	s_nop 0
	global_load_lds_dwordx4 v124, s[26:27]
	v_mfma_f32_32x32x64_f8f6f4 v[64:79], v[24:29], v[96:101], 0 cbsz:2 blgp:2
	ds_read_b128 v[0:3], v124 offset:12288
	ds_read_b64 v[4:5], v125 offset:16384
	ds_read_b128 v[6:9], v124 offset:13312
	ds_read_b64 v[10:11], v125 offset:16896
	ds_read_b128 v[24:27], v124 offset:18432
	ds_read_b64 v[28:29], v125 offset:22528
	v_mfma_f32_32x32x64_f8f6f4 v[64:79], v[30:35], v[102:107], v[64:79] cbsz:2 blgp:2
	ds_read_b128 v[12:15], v124 offset:14336
	ds_read_b64 v[16:17], v125 offset:17408
	ds_read_b128 v[18:21], v124 offset:15360
	ds_read_b64 v[22:23], v125 offset:17920
	ds_read_b128 v[30:33], v124 offset:19456
	ds_read_b64 v[34:35], v125 offset:23040
	v_exp_f32_e32 v48, v48
	v_exp_f32_e32 v49, v49
	v_exp_f32_e32 v50, v50
	v_exp_f32_e32 v51, v51
	v_mfma_f32_32x32x64_f8f6f4 v[64:79], v[36:41], v[108:113], v[64:79] cbsz:2 blgp:2
	ds_read_b128 v[36:39], v124 offset:20480
	ds_read_b64 v[40:41], v125 offset:23552
	v_exp_f32_e32 v52, v52
	v_exp_f32_e32 v53, v53
	v_exp_f32_e32 v54, v54
	v_exp_f32_e32 v55, v55
	v_pk_add_f32 v[120:121], v[120:121], v[48:49]
	v_pk_add_f32 v[122:123], v[122:123], v[50:51]
	v_mfma_f32_32x32x64_f8f6f4 v[64:79], v[42:47], v[114:119], v[64:79] cbsz:2 blgp:2
	ds_read_b128 v[42:45], v124 offset:21504
	ds_read_b64 v[46:47], v125 offset:24064
	v_exp_f32_e32 v56, v56
	v_exp_f32_e32 v57, v57
	v_exp_f32_e32 v58, v58
	v_exp_f32_e32 v59, v59
	v_pk_add_f32 v[120:121], v[120:121], v[52:53]
	v_pk_add_f32 v[122:123], v[122:123], v[54:55]
	s_waitcnt vmcnt(6) lgkmcnt(6)
	s_barrier
	v_mfma_f32_32x32x64_f8f6f4 v[80:95], v[0:5], v[96:101], 0 cbsz:2 blgp:2
	ds_read_b128 v[0:3], v124 offset:24576
	ds_read_b64 v[4:5], v125 offset:28672
	v_exp_f32_e32 v60, v60
	v_exp_f32_e32 v61, v61
	v_exp_f32_e32 v62, v62
	v_exp_f32_e32 v63, v63
	v_pk_add_f32 v[120:121], v[120:121], v[56:57]
	v_pk_add_f32 v[122:123], v[122:123], v[58:59]
	v_mfma_f32_32x32x64_f8f6f4 v[80:95], v[6:11], v[102:107], v[80:95] cbsz:2 blgp:2
	ds_read_b128 v[6:9], v124 offset:25600
	ds_read_b64 v[10:11], v125 offset:29184
	v_exp_f32_e32 v64, v64
	v_exp_f32_e32 v65, v65
	v_exp_f32_e32 v66, v66
	v_exp_f32_e32 v67, v67
	v_pk_add_f32 v[120:121], v[120:121], v[60:61]
	v_pk_add_f32 v[122:123], v[122:123], v[62:63]
	v_mfma_f32_32x32x64_f8f6f4 v[80:95], v[12:17], v[108:113], v[80:95] cbsz:2 blgp:2
	ds_read_b128 v[12:15], v124 offset:26624
	ds_read_b64 v[16:17], v125 offset:29696
	v_exp_f32_e32 v68, v68
	v_exp_f32_e32 v69, v69
	v_exp_f32_e32 v70, v70
	v_exp_f32_e32 v71, v71
	v_pk_add_f32 v[120:121], v[120:121], v[64:65]
	v_pk_add_f32 v[122:123], v[122:123], v[66:67]
	v_mfma_f32_32x32x64_f8f6f4 v[80:95], v[18:23], v[114:119], v[80:95] cbsz:2 blgp:2
	ds_read_b128 v[18:21], v124 offset:27648
	ds_read_b64 v[22:23], v125 offset:30208
	v_exp_f32_e32 v72, v72
	v_exp_f32_e32 v73, v73
	v_exp_f32_e32 v74, v74
	v_exp_f32_e32 v75, v75
	v_pk_add_f32 v[120:121], v[120:121], v[68:69]
	v_pk_add_f32 v[122:123], v[122:123], v[70:71]
	s_waitcnt lgkmcnt(8)
	v_mfma_f32_32x32x64_f8f6f4 v[48:63], v[24:29], v[96:101], 0 cbsz:2 blgp:2
	ds_read_b128 v[24:27], v124 offset:30720
	ds_read_b64 v[28:29], v125 offset:34816
	v_exp_f32_e32 v76, v76
	v_exp_f32_e32 v77, v77
	v_exp_f32_e32 v78, v78
	v_exp_f32_e32 v79, v79
	v_pk_add_f32 v[120:121], v[120:121], v[72:73]
	v_pk_add_f32 v[122:123], v[122:123], v[74:75]
	v_mfma_f32_32x32x64_f8f6f4 v[48:63], v[30:35], v[102:107], v[48:63] cbsz:2 blgp:2
	ds_read_b128 v[30:33], v124 offset:31744
	ds_read_b64 v[34:35], v125 offset:35328
	v_exp_f32_e32 v80, v80
	v_exp_f32_e32 v81, v81
	v_exp_f32_e32 v82, v82
	v_exp_f32_e32 v83, v83
	v_pk_add_f32 v[120:121], v[120:121], v[76:77]
	v_pk_add_f32 v[122:123], v[122:123], v[78:79]
	v_mfma_f32_32x32x64_f8f6f4 v[48:63], v[36:41], v[108:113], v[48:63] cbsz:2 blgp:2
	ds_read_b128 v[36:39], v124 offset:32768
	ds_read_b64 v[40:41], v125 offset:35840
	v_exp_f32_e32 v84, v84
	v_exp_f32_e32 v85, v85
	v_exp_f32_e32 v86, v86
	v_exp_f32_e32 v87, v87
	v_pk_add_f32 v[120:121], v[120:121], v[80:81]
	v_pk_add_f32 v[122:123], v[122:123], v[82:83]
	v_mfma_f32_32x32x64_f8f6f4 v[48:63], v[42:47], v[114:119], v[48:63] cbsz:2 blgp:2
	ds_read_b128 v[42:45], v124 offset:33792
	ds_read_b64 v[46:47], v125 offset:36352
	v_exp_f32_e32 v88, v88
	v_exp_f32_e32 v89, v89
	v_exp_f32_e32 v90, v90
	v_exp_f32_e32 v91, v91
	v_pk_add_f32 v[120:121], v[120:121], v[84:85]
	v_pk_add_f32 v[122:123], v[122:123], v[86:87]
	s_setprio 1
	s_waitcnt vmcnt(4) lgkmcnt(8)
	s_barrier
	v_mfma_f32_32x32x64_f8f6f4 v[64:79], v[0:5], v[96:101], 0 cbsz:2 blgp:2
	ds_read_b128 v[0:3], v124 offset:36864
	ds_read_b64 v[4:5], v125 offset:40960
	v_exp_f32_e32 v92, v92
	v_exp_f32_e32 v93, v93
	v_exp_f32_e32 v94, v94
	v_exp_f32_e32 v95, v95
	v_pk_add_f32 v[120:121], v[120:121], v[88:89]
	v_pk_add_f32 v[122:123], v[122:123], v[90:91]
	v_mfma_f32_32x32x64_f8f6f4 v[64:79], v[6:11], v[102:107], v[64:79] cbsz:2 blgp:2
	ds_read_b128 v[6:9], v124 offset:37888
	ds_read_b64 v[10:11], v125 offset:41472
	v_exp_f32_e32 v48, v48
	v_exp_f32_e32 v49, v49
	v_exp_f32_e32 v50, v50
	v_exp_f32_e32 v51, v51
	v_pk_add_f32 v[120:121], v[120:121], v[92:93]
	v_pk_add_f32 v[122:123], v[122:123], v[94:95]
	v_mfma_f32_32x32x64_f8f6f4 v[64:79], v[12:17], v[108:113], v[64:79] cbsz:2 blgp:2
	ds_read_b128 v[12:15], v124 offset:38912
	ds_read_b64 v[16:17], v125 offset:41984
	v_exp_f32_e32 v52, v52
	v_exp_f32_e32 v53, v53
	v_exp_f32_e32 v54, v54
	v_exp_f32_e32 v55, v55
	v_pk_add_f32 v[120:121], v[120:121], v[48:49]
	v_pk_add_f32 v[122:123], v[122:123], v[50:51]
	v_mfma_f32_32x32x64_f8f6f4 v[64:79], v[18:23], v[114:119], v[64:79] cbsz:2 blgp:2
	ds_read_b128 v[18:21], v124 offset:39936
	ds_read_b64 v[22:23], v125 offset:42496
	v_exp_f32_e32 v56, v56
	v_exp_f32_e32 v57, v57
	v_exp_f32_e32 v58, v58
	v_exp_f32_e32 v59, v59
	v_pk_add_f32 v[120:121], v[120:121], v[52:53]
	v_pk_add_f32 v[122:123], v[122:123], v[54:55]
	s_waitcnt lgkmcnt(8)
	v_mfma_f32_32x32x64_f8f6f4 v[80:95], v[24:29], v[96:101], 0 cbsz:2 blgp:2
	ds_read_b128 v[24:27], v124 offset:43008
	ds_read_b64 v[28:29], v125 offset:47104
	v_exp_f32_e32 v60, v60
	v_exp_f32_e32 v61, v61
	v_exp_f32_e32 v62, v62
	v_exp_f32_e32 v63, v63
	v_pk_add_f32 v[120:121], v[120:121], v[56:57]
	v_pk_add_f32 v[122:123], v[122:123], v[58:59]
	v_mfma_f32_32x32x64_f8f6f4 v[80:95], v[30:35], v[102:107], v[80:95] cbsz:2 blgp:2
	ds_read_b128 v[30:33], v124 offset:44032
	ds_read_b64 v[34:35], v125 offset:47616
	v_exp_f32_e32 v64, v64
	v_exp_f32_e32 v65, v65
	v_exp_f32_e32 v66, v66
	v_exp_f32_e32 v67, v67
	v_pk_add_f32 v[120:121], v[120:121], v[60:61]
	v_pk_add_f32 v[122:123], v[122:123], v[62:63]
	v_mfma_f32_32x32x64_f8f6f4 v[80:95], v[36:41], v[108:113], v[80:95] cbsz:2 blgp:2
	ds_read_b128 v[36:39], v124 offset:45056
	ds_read_b64 v[40:41], v125 offset:48128
	v_exp_f32_e32 v68, v68
	v_exp_f32_e32 v69, v69
	v_exp_f32_e32 v70, v70
	v_exp_f32_e32 v71, v71
	v_pk_add_f32 v[120:121], v[120:121], v[64:65]
	v_pk_add_f32 v[122:123], v[122:123], v[66:67]
	v_mfma_f32_32x32x64_f8f6f4 v[80:95], v[42:47], v[114:119], v[80:95] cbsz:2 blgp:2
	ds_read_b128 v[42:45], v124 offset:46080
	ds_read_b64 v[46:47], v125 offset:48640
	v_exp_f32_e32 v72, v72
	v_exp_f32_e32 v73, v73
	v_exp_f32_e32 v74, v74
	v_exp_f32_e32 v75, v75
	v_pk_add_f32 v[120:121], v[120:121], v[68:69]
	v_pk_add_f32 v[122:123], v[122:123], v[70:71]
	s_waitcnt vmcnt(2) lgkmcnt(8)
	s_barrier
	v_mfma_f32_32x32x64_f8f6f4 v[48:63], v[0:5], v[96:101], 0 cbsz:2 blgp:2
	ds_read_b128 v[0:3], v124 offset:49152
	ds_read_b64 v[4:5], v125 offset:53248
	v_exp_f32_e32 v76, v76
	v_exp_f32_e32 v77, v77
	v_exp_f32_e32 v78, v78
	v_exp_f32_e32 v79, v79
	v_pk_add_f32 v[120:121], v[120:121], v[72:73]
	v_pk_add_f32 v[122:123], v[122:123], v[74:75]
	v_mfma_f32_32x32x64_f8f6f4 v[48:63], v[6:11], v[102:107], v[48:63] cbsz:2 blgp:2
	ds_read_b128 v[6:9], v124 offset:50176
	ds_read_b64 v[10:11], v125 offset:53760
	v_exp_f32_e32 v80, v80
	v_exp_f32_e32 v81, v81
	v_exp_f32_e32 v82, v82
	v_exp_f32_e32 v83, v83
	v_pk_add_f32 v[120:121], v[120:121], v[76:77]
	v_pk_add_f32 v[122:123], v[122:123], v[78:79]
	v_mfma_f32_32x32x64_f8f6f4 v[48:63], v[12:17], v[108:113], v[48:63] cbsz:2 blgp:2
	ds_read_b128 v[12:15], v124 offset:51200
	ds_read_b64 v[16:17], v125 offset:54272
	v_exp_f32_e32 v84, v84
	v_exp_f32_e32 v85, v85
	v_exp_f32_e32 v86, v86
	v_exp_f32_e32 v87, v87
	v_pk_add_f32 v[120:121], v[120:121], v[80:81]
	v_pk_add_f32 v[122:123], v[122:123], v[82:83]
	v_mfma_f32_32x32x64_f8f6f4 v[48:63], v[18:23], v[114:119], v[48:63] cbsz:2 blgp:2
	ds_read_b128 v[18:21], v124 offset:52224
	ds_read_b64 v[22:23], v125 offset:54784
	v_exp_f32_e32 v88, v88
	v_exp_f32_e32 v89, v89
	v_exp_f32_e32 v90, v90
	v_exp_f32_e32 v91, v91
	v_pk_add_f32 v[120:121], v[120:121], v[84:85]
	v_pk_add_f32 v[122:123], v[122:123], v[86:87]
	s_waitcnt lgkmcnt(8)
	v_mfma_f32_32x32x64_f8f6f4 v[64:79], v[24:29], v[96:101], 0 cbsz:2 blgp:2
	ds_read_b128 v[24:27], v124 offset:55296
	ds_read_b64 v[28:29], v125 offset:59392
	v_exp_f32_e32 v92, v92
	v_exp_f32_e32 v93, v93
	v_exp_f32_e32 v94, v94
	v_exp_f32_e32 v95, v95
	v_pk_add_f32 v[120:121], v[120:121], v[88:89]
	v_pk_add_f32 v[122:123], v[122:123], v[90:91]
	v_mfma_f32_32x32x64_f8f6f4 v[64:79], v[30:35], v[102:107], v[64:79] cbsz:2 blgp:2
	ds_read_b128 v[30:33], v124 offset:56320
	ds_read_b64 v[34:35], v125 offset:59904
	v_exp_f32_e32 v48, v48
	v_exp_f32_e32 v49, v49
	v_exp_f32_e32 v50, v50
	v_exp_f32_e32 v51, v51
	v_pk_add_f32 v[120:121], v[120:121], v[92:93]
	v_pk_add_f32 v[122:123], v[122:123], v[94:95]
	v_mfma_f32_32x32x64_f8f6f4 v[64:79], v[36:41], v[108:113], v[64:79] cbsz:2 blgp:2
	ds_read_b128 v[36:39], v124 offset:57344
	ds_read_b64 v[40:41], v125 offset:60416
	v_exp_f32_e32 v52, v52
	v_exp_f32_e32 v53, v53
	v_exp_f32_e32 v54, v54
	v_exp_f32_e32 v55, v55
	v_pk_add_f32 v[120:121], v[120:121], v[48:49]
	v_pk_add_f32 v[122:123], v[122:123], v[50:51]
	v_mfma_f32_32x32x64_f8f6f4 v[64:79], v[42:47], v[114:119], v[64:79] cbsz:2 blgp:2
	ds_read_b128 v[42:45], v124 offset:58368
	ds_read_b64 v[46:47], v125 offset:60928
	v_exp_f32_e32 v56, v56
	v_exp_f32_e32 v57, v57
	v_exp_f32_e32 v58, v58
	v_exp_f32_e32 v59, v59
	v_pk_add_f32 v[120:121], v[120:121], v[52:53]
	v_pk_add_f32 v[122:123], v[122:123], v[54:55]
	s_setprio 0
	s_waitcnt vmcnt(0) lgkmcnt(8)
	s_barrier
	v_mfma_f32_32x32x64_f8f6f4 v[80:95], v[0:5], v[96:101], 0 cbsz:2 blgp:2
	ds_read_b128 v[0:3], v124
	ds_read_b64 v[4:5], v125 offset:4096
	v_exp_f32_e32 v60, v60
	v_exp_f32_e32 v61, v61
	v_exp_f32_e32 v62, v62
	v_exp_f32_e32 v63, v63
	v_pk_add_f32 v[120:121], v[120:121], v[56:57]
	v_pk_add_f32 v[122:123], v[122:123], v[58:59]
	v_mfma_f32_32x32x64_f8f6f4 v[80:95], v[6:11], v[102:107], v[80:95] cbsz:2 blgp:2
	ds_read_b128 v[6:9], v124 offset:1024
	ds_read_b64 v[10:11], v125 offset:4608
	v_exp_f32_e32 v64, v64
	v_exp_f32_e32 v65, v65
	v_exp_f32_e32 v66, v66
	v_exp_f32_e32 v67, v67
	v_pk_add_f32 v[120:121], v[120:121], v[60:61]
	v_pk_add_f32 v[122:123], v[122:123], v[62:63]
	v_mfma_f32_32x32x64_f8f6f4 v[80:95], v[12:17], v[108:113], v[80:95] cbsz:2 blgp:2
	ds_read_b128 v[12:15], v124 offset:2048
	ds_read_b64 v[16:17], v125 offset:5120
	v_exp_f32_e32 v68, v68
	v_exp_f32_e32 v69, v69
	v_exp_f32_e32 v70, v70
	v_exp_f32_e32 v71, v71
	v_pk_add_f32 v[120:121], v[120:121], v[64:65]
	v_pk_add_f32 v[122:123], v[122:123], v[66:67]
	v_mfma_f32_32x32x64_f8f6f4 v[80:95], v[18:23], v[114:119], v[80:95] cbsz:2 blgp:2
	ds_read_b128 v[18:21], v124 offset:3072
	ds_read_b64 v[22:23], v125 offset:5632
	v_exp_f32_e32 v72, v72
	v_exp_f32_e32 v73, v73
	v_exp_f32_e32 v74, v74
	v_exp_f32_e32 v75, v75
	v_pk_add_f32 v[120:121], v[120:121], v[68:69]
	v_pk_add_f32 v[122:123], v[122:123], v[70:71]
	s_waitcnt lgkmcnt(8)
	v_mfma_f32_32x32x64_f8f6f4 v[48:63], v[24:29], v[96:101], 0 cbsz:2 blgp:2
	ds_read_b128 v[24:27], v124 offset:6144
	ds_read_b64 v[28:29], v125 offset:10240
	v_exp_f32_e32 v76, v76
	v_exp_f32_e32 v77, v77
	v_exp_f32_e32 v78, v78
	v_exp_f32_e32 v79, v79
	v_pk_add_f32 v[120:121], v[120:121], v[72:73]
	v_pk_add_f32 v[122:123], v[122:123], v[74:75]
	v_mfma_f32_32x32x64_f8f6f4 v[48:63], v[30:35], v[102:107], v[48:63] cbsz:2 blgp:2
	ds_read_b128 v[30:33], v124 offset:7168
	ds_read_b64 v[34:35], v125 offset:10752
	v_exp_f32_e32 v80, v80
	v_exp_f32_e32 v81, v81
	v_exp_f32_e32 v82, v82
	v_exp_f32_e32 v83, v83
	v_pk_add_f32 v[120:121], v[120:121], v[76:77]
	v_pk_add_f32 v[122:123], v[122:123], v[78:79]
	s_cmp_lg_u32 s8, 10
	s_cbranch_scc1 .Lmk_nosplit_a
	v_add_f32_e32 v127, v120, v121
	v_add_f32_e32 v126, v122, v123
	v_mov_b32_e32 v120, 0
	v_mov_b32_e32 v121, 0
	v_mov_b32_e32 v122, 0
	v_mov_b32_e32 v123, 0
	v_add_f32_e32 v127, v127, v126
.Lmk_nosplit_a:
	v_mfma_f32_32x32x64_f8f6f4 v[48:63], v[36:41], v[108:113], v[48:63] cbsz:2 blgp:2
	ds_read_b128 v[36:39], v124 offset:8192
	ds_read_b64 v[40:41], v125 offset:11264
	v_exp_f32_e32 v84, v84
	v_exp_f32_e32 v85, v85
	v_exp_f32_e32 v86, v86
	v_exp_f32_e32 v87, v87
	v_pk_add_f32 v[120:121], v[120:121], v[80:81]
	v_pk_add_f32 v[122:123], v[122:123], v[82:83]
	v_mfma_f32_32x32x64_f8f6f4 v[48:63], v[42:47], v[114:119], v[48:63] cbsz:2 blgp:2
	ds_read_b128 v[42:45], v124 offset:9216
	ds_read_b64 v[46:47], v125 offset:11776
	v_exp_f32_e32 v88, v88
	v_exp_f32_e32 v89, v89
	v_exp_f32_e32 v90, v90
	v_exp_f32_e32 v91, v91
	v_pk_add_f32 v[120:121], v[120:121], v[84:85]
	v_pk_add_f32 v[122:123], v[122:123], v[86:87]
	s_waitcnt lgkmcnt(8)
	v_mfma_f32_32x32x64_f8f6f4 v[64:79], v[0:5], v[96:101], 0 cbsz:2 blgp:2
	v_exp_f32_e32 v92, v92
	v_exp_f32_e32 v93, v93
	v_exp_f32_e32 v94, v94
	v_exp_f32_e32 v95, v95
	v_pk_add_f32 v[120:121], v[120:121], v[88:89]
	v_pk_add_f32 v[122:123], v[122:123], v[90:91]
	v_mfma_f32_32x32x64_f8f6f4 v[64:79], v[6:11], v[102:107], v[64:79] cbsz:2 blgp:2
	v_exp_f32_e32 v48, v48
	v_exp_f32_e32 v49, v49
	v_exp_f32_e32 v50, v50
	v_exp_f32_e32 v51, v51
	v_pk_add_f32 v[120:121], v[120:121], v[92:93]
	v_pk_add_f32 v[122:123], v[122:123], v[94:95]
	v_mfma_f32_32x32x64_f8f6f4 v[64:79], v[12:17], v[108:113], v[64:79] cbsz:2 blgp:2
	v_exp_f32_e32 v52, v52
	v_exp_f32_e32 v53, v53
	v_exp_f32_e32 v54, v54
	v_exp_f32_e32 v55, v55
	v_pk_add_f32 v[120:121], v[120:121], v[48:49]
	v_pk_add_f32 v[122:123], v[122:123], v[50:51]
	v_mfma_f32_32x32x64_f8f6f4 v[64:79], v[18:23], v[114:119], v[64:79] cbsz:2 blgp:2
	v_exp_f32_e32 v56, v56
	v_exp_f32_e32 v57, v57
	v_exp_f32_e32 v58, v58
	v_exp_f32_e32 v59, v59
	v_pk_add_f32 v[120:121], v[120:121], v[52:53]
	v_pk_add_f32 v[122:123], v[122:123], v[54:55]
	s_waitcnt lgkmcnt(0)
	v_mfma_f32_32x32x64_f8f6f4 v[80:95], v[24:29], v[96:101], 0 cbsz:2 blgp:2
	v_exp_f32_e32 v60, v60
	v_exp_f32_e32 v61, v61
	v_exp_f32_e32 v62, v62
	v_exp_f32_e32 v63, v63
	v_pk_add_f32 v[120:121], v[120:121], v[56:57]
	v_pk_add_f32 v[122:123], v[122:123], v[58:59]
	v_mfma_f32_32x32x64_f8f6f4 v[80:95], v[30:35], v[102:107], v[80:95] cbsz:2 blgp:2
	v_exp_f32_e32 v64, v64
	v_exp_f32_e32 v65, v65
	v_exp_f32_e32 v66, v66
	v_exp_f32_e32 v67, v67
	v_pk_add_f32 v[120:121], v[120:121], v[60:61]
	v_pk_add_f32 v[122:123], v[122:123], v[62:63]
	v_mfma_f32_32x32x64_f8f6f4 v[80:95], v[36:41], v[108:113], v[80:95] cbsz:2 blgp:2
	v_exp_f32_e32 v68, v68
	v_exp_f32_e32 v69, v69
	v_exp_f32_e32 v70, v70
	v_exp_f32_e32 v71, v71
	v_pk_add_f32 v[120:121], v[120:121], v[64:65]
	v_pk_add_f32 v[122:123], v[122:123], v[66:67]
	v_mfma_f32_32x32x64_f8f6f4 v[80:95], v[42:47], v[114:119], v[80:95] cbsz:2 blgp:2
	v_exp_f32_e32 v72, v72
	v_exp_f32_e32 v73, v73
	v_exp_f32_e32 v74, v74
	v_exp_f32_e32 v75, v75
	v_pk_add_f32 v[120:121], v[120:121], v[68:69]
	v_pk_add_f32 v[122:123], v[122:123], v[70:71]
	v_exp_f32_e32 v76, v76
	v_exp_f32_e32 v77, v77
	v_exp_f32_e32 v78, v78
	v_exp_f32_e32 v79, v79
	v_pk_add_f32 v[120:121], v[120:121], v[72:73]
	v_pk_add_f32 v[122:123], v[122:123], v[74:75]
	s_nop 1
	v_exp_f32_e32 v80, v80
	v_exp_f32_e32 v81, v81
	v_exp_f32_e32 v82, v82
	v_exp_f32_e32 v83, v83
	v_pk_add_f32 v[120:121], v[120:121], v[76:77]
	v_pk_add_f32 v[122:123], v[122:123], v[78:79]
	v_exp_f32_e32 v84, v84
	v_exp_f32_e32 v85, v85
	v_exp_f32_e32 v86, v86
	v_exp_f32_e32 v87, v87
	v_pk_add_f32 v[120:121], v[120:121], v[80:81]
	v_pk_add_f32 v[122:123], v[122:123], v[82:83]
	v_exp_f32_e32 v88, v88
	v_exp_f32_e32 v89, v89
	v_exp_f32_e32 v90, v90
	v_exp_f32_e32 v91, v91
	v_pk_add_f32 v[120:121], v[120:121], v[84:85]
	v_pk_add_f32 v[122:123], v[122:123], v[86:87]
	v_exp_f32_e32 v92, v92
	v_exp_f32_e32 v93, v93
	v_exp_f32_e32 v94, v94
	v_exp_f32_e32 v95, v95
	v_pk_add_f32 v[120:121], v[120:121], v[88:89]
	v_pk_add_f32 v[122:123], v[122:123], v[90:91]
	v_pk_add_f32 v[120:121], v[120:121], v[92:93]
	v_pk_add_f32 v[122:123], v[122:123], v[94:95]
	v_add_f32_e32 v120, v120, v121
	v_add_f32_e32 v122, v122, v123
	v_lshrrev_b32_e32 v126, 2, v124
	v_add_f32_e32 v120, v120, v122
	v_xor_b32_e32 v125, 0x80, v126
	s_mov_b64 s[4:5], s[30:31]
	s_mov_b64 s[6:7], s[32:33]
	ds_bpermute_b32 v122, v125, v120
	ds_bpermute_b32 v123, v125, v127
	s_lshl_b32 s14, s14, 7
	v_add_u32_e32 v126, s14, v126
	v_cmp_gt_u32_e32 vcc, 0x200, v124
	s_and_saveexec_b64 s[16:17], vcc
	s_cbranch_execz .Lmk_end_a
	s_waitcnt lgkmcnt(0)
	v_add_f32_e32 v120, v120, v122
	v_add_f32_e32 v127, v127, v123
	s_cmp_lt_u32 s8, 10
	s_cbranch_scc1 .Lmk_pos_only_a
	s_cmp_eq_u32 s8, 10
	s_cbranch_scc0 .Lmk_neg_only_a
	global_atomic_add_f32 v126, v127, s[4:5]
